# P7b router: group and expert logit dot products rewritten as 4-accumulator v_fmac chains with all LDS/L2 loads issued up front (f32, same math)
# speedup vs baseline: 1.0116x; 1.0001x over previous
.LBB0_790:
	global_load_dword v111, v3, s[14:15]
	ds_read_b128 v[190:193], v100
	ds_read_b128 v[194:197], v100 offset:1024
	ds_read_b128 v[198:201], v100 offset:2048
	ds_read_b128 v[202:205], v100 offset:3072
	ds_read_b128 v[206:209], v100 offset:4096
	ds_read_b128 v[210:213], v100 offset:5120
	ds_read_b128 v[214:217], v100 offset:6144
	ds_read_b128 v[218:221], v100 offset:7168
	ds_read_b128 v[222:225], v100 offset:8192
	ds_read_b128 v[226:229], v100 offset:9216
	ds_read_b128 v[232:235], v100 offset:10240
	ds_read_b128 v[236:239], v100 offset:11264
	ds_read_b128 v[240:243], v100 offset:12288
	ds_read_b128 v[244:247], v100 offset:13312
	ds_read_b128 v[248:251], v100 offset:14336
	s_waitcnt lgkmcnt(14)
	v_mul_f32_e32 v104, v190, v38
	v_mul_f32_e32 v105, v191, v39
	v_mul_f32_e32 v106, v192, v36
	v_mul_f32_e32 v107, v193, v37
	ds_read_b128 v[184:187], v100 offset:15360
	s_waitcnt lgkmcnt(14)
	v_fmac_f32_e32 v104, v194, v42
	v_fmac_f32_e32 v105, v195, v43
	v_fmac_f32_e32 v106, v196, v40
	v_fmac_f32_e32 v107, v197, v41
	s_waitcnt lgkmcnt(13)
	v_fmac_f32_e32 v104, v198, v46
	v_fmac_f32_e32 v105, v199, v47
	v_fmac_f32_e32 v106, v200, v44
	v_fmac_f32_e32 v107, v201, v45
	s_waitcnt lgkmcnt(12)
	v_fmac_f32_e32 v104, v202, v50
	v_fmac_f32_e32 v105, v203, v51
	v_fmac_f32_e32 v106, v204, v48
	v_fmac_f32_e32 v107, v205, v49
	s_waitcnt lgkmcnt(11)
	v_fmac_f32_e32 v104, v206, v54
	v_fmac_f32_e32 v105, v207, v55
	v_fmac_f32_e32 v106, v208, v52
	v_fmac_f32_e32 v107, v209, v53
	s_waitcnt lgkmcnt(10)
	v_fmac_f32_e32 v104, v210, v58
	v_fmac_f32_e32 v105, v211, v59
	v_fmac_f32_e32 v106, v212, v56
	v_fmac_f32_e32 v107, v213, v57
	s_waitcnt lgkmcnt(9)
	v_fmac_f32_e32 v104, v214, v62
	v_fmac_f32_e32 v105, v215, v63
	v_fmac_f32_e32 v106, v216, v60
	v_fmac_f32_e32 v107, v217, v61
	s_waitcnt lgkmcnt(8)
	v_fmac_f32_e32 v104, v218, v66
	v_fmac_f32_e32 v105, v219, v67
	v_fmac_f32_e32 v106, v220, v64
	v_fmac_f32_e32 v107, v221, v65
	s_waitcnt lgkmcnt(7)
	v_fmac_f32_e32 v104, v222, v70
	v_fmac_f32_e32 v105, v223, v71
	v_fmac_f32_e32 v106, v224, v68
	v_fmac_f32_e32 v107, v225, v69
	s_waitcnt lgkmcnt(6)
	v_fmac_f32_e32 v104, v226, v74
	v_fmac_f32_e32 v105, v227, v75
	v_fmac_f32_e32 v106, v228, v72
	v_fmac_f32_e32 v107, v229, v73
	s_waitcnt lgkmcnt(5)
	v_fmac_f32_e32 v104, v232, v78
	v_fmac_f32_e32 v105, v233, v79
	v_fmac_f32_e32 v106, v234, v76
	v_fmac_f32_e32 v107, v235, v77
	s_waitcnt lgkmcnt(4)
	v_fmac_f32_e32 v104, v236, v82
	v_fmac_f32_e32 v105, v237, v83
	v_fmac_f32_e32 v106, v238, v80
	v_fmac_f32_e32 v107, v239, v81
	s_waitcnt lgkmcnt(3)
	v_fmac_f32_e32 v104, v240, v86
	v_fmac_f32_e32 v105, v241, v87
	v_fmac_f32_e32 v106, v242, v84
	v_fmac_f32_e32 v107, v243, v85
	s_waitcnt lgkmcnt(2)
	v_fmac_f32_e32 v104, v244, v90
	v_fmac_f32_e32 v105, v245, v91
	v_fmac_f32_e32 v106, v246, v88
	v_fmac_f32_e32 v107, v247, v89
	s_waitcnt lgkmcnt(1)
	v_fmac_f32_e32 v104, v248, v94
	v_fmac_f32_e32 v105, v249, v95
	v_fmac_f32_e32 v106, v250, v92
	v_fmac_f32_e32 v107, v251, v93
	s_waitcnt lgkmcnt(0)
	v_fmac_f32_e32 v104, v184, v98
	v_fmac_f32_e32 v105, v185, v99
	v_fmac_f32_e32 v106, v186, v96
	v_fmac_f32_e32 v107, v187, v97
	v_add_f32_e32 v104, v104, v105
	v_add_f32_e32 v106, v106, v107
	v_add_f32_e32 v103, v104, v106
	s_nop 1
	v_add_f32_dpp v103, v103, v103 quad_perm:[1,0,3,2] row_mask:0xf bank_mask:0xf bound_ctrl:1
	s_nop 1
	v_add_f32_dpp v103, v103, v103 quad_perm:[2,3,0,1] row_mask:0xf bank_mask:0xf bound_ctrl:1
	s_nop 1
	v_add_f32_dpp v103, v103, v103 row_half_mirror row_mask:0xf bank_mask:0xf bound_ctrl:1
	s_nop 1
	v_add_f32_dpp v103, v103, v103 row_mirror row_mask:0xf bank_mask:0xf bound_ctrl:1
	s_nop 0
	v_readlane_b32 s34, v103, 16
	v_readlane_b32 s35, v103, 48
	v_readlane_b32 s16, v103, 0
	v_readlane_b32 s17, v103, 32
	v_mov_b32_e32 v104, s34
	v_mov_b32_e32 v105, s35
	v_pk_add_f32 v[104:105], s[16:17], v[104:105]
	s_nop 0
	v_add_f32_e32 v103, v104, v105
	s_waitcnt vmcnt(0)
	v_add_f32_e32 v103, v111, v103
	v_cmp_ngt_f32_e32 vcc, v103, v101
	s_cbranch_vccz .LBB0_792
	v_sub_f32_e32 v104, v103, v101
	v_mul_f32_e32 v104, 0x3fb8aa3b, v104
	v_exp_f32_e32 v104, v104
	s_nop 0
	v_add_f32_e32 v104, v102, v104
	s_cbranch_execz .LBB0_793
	s_branch .LBB0_794

.LBB0_797:
	s_add_i32 s36, s35, 2
	global_load_dwordx2 v[102:103], v3, s[14:15] offset:-4
	v_add_co_u32_e32 v112, vcc, 0xffff9400, v100
	s_nop 1
	v_addc_co_u32_e32 v113, vcc, -1, v101, vcc
	v_add_co_u32_e32 v114, vcc, 0xffffb400, v100
	s_nop 1
	v_addc_co_u32_e32 v115, vcc, -1, v101, vcc
	v_add_co_u32_e32 v184, vcc, 0xffffd400, v100
	s_nop 1
	v_addc_co_u32_e32 v185, vcc, -1, v101, vcc
	v_add_co_u32_e32 v186, vcc, 0xfffff400, v100
	s_nop 1
	v_addc_co_u32_e32 v187, vcc, -1, v101, vcc
	global_load_dwordx4 v[116:119], v[112:113], off offset:-4096
	global_load_dwordx4 v[190:193], v[184:185], off offset:-4096
	global_load_dwordx4 v[120:123], v[112:113], off offset:-3072
	global_load_dwordx4 v[194:197], v[184:185], off offset:-3072
	global_load_dwordx4 v[124:127], v[112:113], off offset:-2048
	global_load_dwordx4 v[198:201], v[184:185], off offset:-2048
	global_load_dwordx4 v[128:131], v[112:113], off offset:-1024
	global_load_dwordx4 v[202:205], v[184:185], off offset:-1024
	global_load_dwordx4 v[132:135], v[112:113], off
	global_load_dwordx4 v[206:209], v[184:185], off
	global_load_dwordx4 v[136:139], v[112:113], off offset:1024
	global_load_dwordx4 v[210:213], v[184:185], off offset:1024
	global_load_dwordx4 v[140:143], v[112:113], off offset:2048
	global_load_dwordx4 v[214:217], v[184:185], off offset:2048
	global_load_dwordx4 v[144:147], v[112:113], off offset:3072
	global_load_dwordx4 v[218:221], v[184:185], off offset:3072
	global_load_dwordx4 v[148:151], v[114:115], off offset:-4096
	global_load_dwordx4 v[222:225], v[186:187], off offset:-4096
	global_load_dwordx4 v[152:155], v[114:115], off offset:-3072
	global_load_dwordx4 v[226:229], v[186:187], off offset:-3072
	global_load_dwordx4 v[156:159], v[114:115], off offset:-2048
	global_load_dwordx4 v[232:235], v[186:187], off offset:-2048
	global_load_dwordx4 v[160:163], v[114:115], off offset:-1024
	global_load_dwordx4 v[236:239], v[186:187], off offset:-1024
	global_load_dwordx4 v[164:167], v[114:115], off
	global_load_dwordx4 v[240:243], v[186:187], off
	global_load_dwordx4 v[168:171], v[114:115], off offset:1024
	global_load_dwordx4 v[244:247], v[186:187], off offset:1024
	global_load_dwordx4 v[172:175], v[114:115], off offset:2048
	global_load_dwordx4 v[248:251], v[186:187], off offset:2048
	global_load_dwordx4 v[176:179], v[114:115], off offset:3072
	global_load_dwordx4 v[180:183], v[186:187], off offset:3072
	s_waitcnt vmcnt(30)
	v_mul_f32_e32 v111, v116, v38
	v_mul_f32_e32 v107, v190, v38
	v_mul_f32_e32 v188, v117, v39
	v_mul_f32_e32 v253, v191, v39
	v_mul_f32_e32 v189, v118, v36
	v_mul_f32_e32 v254, v192, v36
	v_mul_f32_e32 v252, v119, v37
	v_mul_f32_e32 v231, v193, v37
	s_waitcnt vmcnt(28)
	v_fmac_f32_e32 v111, v120, v42
	v_fmac_f32_e32 v107, v194, v42
	v_fmac_f32_e32 v188, v121, v43
	v_fmac_f32_e32 v253, v195, v43
	v_fmac_f32_e32 v189, v122, v40
	v_fmac_f32_e32 v254, v196, v40
	v_fmac_f32_e32 v252, v123, v41
	v_fmac_f32_e32 v231, v197, v41
	s_waitcnt vmcnt(26)
	v_fmac_f32_e32 v111, v124, v46
	v_fmac_f32_e32 v107, v198, v46
	v_fmac_f32_e32 v188, v125, v47
	v_fmac_f32_e32 v253, v199, v47
	v_fmac_f32_e32 v189, v126, v44
	v_fmac_f32_e32 v254, v200, v44
	v_fmac_f32_e32 v252, v127, v45
	v_fmac_f32_e32 v231, v201, v45
	s_waitcnt vmcnt(24)
	v_fmac_f32_e32 v111, v128, v50
	v_fmac_f32_e32 v107, v202, v50
	v_fmac_f32_e32 v188, v129, v51
	v_fmac_f32_e32 v253, v203, v51
	v_fmac_f32_e32 v189, v130, v48
	v_fmac_f32_e32 v254, v204, v48
	v_fmac_f32_e32 v252, v131, v49
	v_fmac_f32_e32 v231, v205, v49
	s_waitcnt vmcnt(22)
	v_fmac_f32_e32 v111, v132, v54
	v_fmac_f32_e32 v107, v206, v54
	v_fmac_f32_e32 v188, v133, v55
	v_fmac_f32_e32 v253, v207, v55
	v_fmac_f32_e32 v189, v134, v52
	v_fmac_f32_e32 v254, v208, v52
	v_fmac_f32_e32 v252, v135, v53
	v_fmac_f32_e32 v231, v209, v53
	s_waitcnt vmcnt(20)
	v_fmac_f32_e32 v111, v136, v58
	v_fmac_f32_e32 v107, v210, v58
	v_fmac_f32_e32 v188, v137, v59
	v_fmac_f32_e32 v253, v211, v59
	v_fmac_f32_e32 v189, v138, v56
	v_fmac_f32_e32 v254, v212, v56
	v_fmac_f32_e32 v252, v139, v57
	v_fmac_f32_e32 v231, v213, v57
	s_waitcnt vmcnt(18)
	v_fmac_f32_e32 v111, v140, v62
	v_fmac_f32_e32 v107, v214, v62
	v_fmac_f32_e32 v188, v141, v63
	v_fmac_f32_e32 v253, v215, v63
	v_fmac_f32_e32 v189, v142, v60
	v_fmac_f32_e32 v254, v216, v60
	v_fmac_f32_e32 v252, v143, v61
	v_fmac_f32_e32 v231, v217, v61
	s_waitcnt vmcnt(16)
	v_fmac_f32_e32 v111, v144, v66
	v_fmac_f32_e32 v107, v218, v66
	v_fmac_f32_e32 v188, v145, v67
	v_fmac_f32_e32 v253, v219, v67
	v_fmac_f32_e32 v189, v146, v64
	v_fmac_f32_e32 v254, v220, v64
	v_fmac_f32_e32 v252, v147, v65
	v_fmac_f32_e32 v231, v221, v65
	s_waitcnt vmcnt(14)
	v_fmac_f32_e32 v111, v148, v70
	v_fmac_f32_e32 v107, v222, v70
	v_fmac_f32_e32 v188, v149, v71
	v_fmac_f32_e32 v253, v223, v71
	v_fmac_f32_e32 v189, v150, v68
	v_fmac_f32_e32 v254, v224, v68
	v_fmac_f32_e32 v252, v151, v69
	v_fmac_f32_e32 v231, v225, v69
	s_waitcnt vmcnt(12)
	v_fmac_f32_e32 v111, v152, v74
	v_fmac_f32_e32 v107, v226, v74
	v_fmac_f32_e32 v188, v153, v75
	v_fmac_f32_e32 v253, v227, v75
	v_fmac_f32_e32 v189, v154, v72
	v_fmac_f32_e32 v254, v228, v72
	v_fmac_f32_e32 v252, v155, v73
	v_fmac_f32_e32 v231, v229, v73
	s_waitcnt vmcnt(10)
	v_fmac_f32_e32 v111, v156, v78
	v_fmac_f32_e32 v107, v232, v78
	v_fmac_f32_e32 v188, v157, v79
	v_fmac_f32_e32 v253, v233, v79
	v_fmac_f32_e32 v189, v158, v76
	v_fmac_f32_e32 v254, v234, v76
	v_fmac_f32_e32 v252, v159, v77
	v_fmac_f32_e32 v231, v235, v77
	s_waitcnt vmcnt(8)
	v_fmac_f32_e32 v111, v160, v82
	v_fmac_f32_e32 v107, v236, v82
	v_fmac_f32_e32 v188, v161, v83
	v_fmac_f32_e32 v253, v237, v83
	v_fmac_f32_e32 v189, v162, v80
	v_fmac_f32_e32 v254, v238, v80
	v_fmac_f32_e32 v252, v163, v81
	v_fmac_f32_e32 v231, v239, v81
	s_waitcnt vmcnt(6)
	v_fmac_f32_e32 v111, v164, v86
	v_fmac_f32_e32 v107, v240, v86
	v_fmac_f32_e32 v188, v165, v87
	v_fmac_f32_e32 v253, v241, v87
	v_fmac_f32_e32 v189, v166, v84
	v_fmac_f32_e32 v254, v242, v84
	v_fmac_f32_e32 v252, v167, v85
	v_fmac_f32_e32 v231, v243, v85
	s_waitcnt vmcnt(4)
	v_fmac_f32_e32 v111, v168, v90
	v_fmac_f32_e32 v107, v244, v90
	v_fmac_f32_e32 v188, v169, v91
	v_fmac_f32_e32 v253, v245, v91
	v_fmac_f32_e32 v189, v170, v88
	v_fmac_f32_e32 v254, v246, v88
	v_fmac_f32_e32 v252, v171, v89
	v_fmac_f32_e32 v231, v247, v89
	s_waitcnt vmcnt(2)
	v_fmac_f32_e32 v111, v172, v94
	v_fmac_f32_e32 v107, v248, v94
	v_fmac_f32_e32 v188, v173, v95
	v_fmac_f32_e32 v253, v249, v95
	v_fmac_f32_e32 v189, v174, v92
	v_fmac_f32_e32 v254, v250, v92
	v_fmac_f32_e32 v252, v175, v93
	v_fmac_f32_e32 v231, v251, v93
	s_waitcnt vmcnt(0)
	v_fmac_f32_e32 v111, v176, v98
	v_fmac_f32_e32 v107, v180, v98
	v_fmac_f32_e32 v188, v177, v99
	v_fmac_f32_e32 v253, v181, v99
	v_fmac_f32_e32 v189, v178, v96
	v_fmac_f32_e32 v254, v182, v96
	v_fmac_f32_e32 v252, v179, v97
	v_fmac_f32_e32 v231, v183, v97
	v_add_f32_e32 v111, v111, v188
	v_add_f32_e32 v189, v189, v252
	v_add_f32_e32 v107, v107, v253
	v_add_f32_e32 v254, v254, v231
	v_add_f32_e32 v111, v111, v189
	v_add_f32_e32 v107, v107, v254
	s_nop 1
	v_add_f32_dpp v111, v111, v111 quad_perm:[1,0,3,2] row_mask:0xf bank_mask:0xf bound_ctrl:1
	v_add_f32_dpp v107, v107, v107 quad_perm:[1,0,3,2] row_mask:0xf bank_mask:0xf bound_ctrl:1
	s_nop 0
	v_add_f32_dpp v111, v111, v111 quad_perm:[2,3,0,1] row_mask:0xf bank_mask:0xf bound_ctrl:1
	v_add_f32_dpp v107, v107, v107 quad_perm:[2,3,0,1] row_mask:0xf bank_mask:0xf bound_ctrl:1
	s_nop 0
	v_add_f32_dpp v111, v111, v111 row_half_mirror row_mask:0xf bank_mask:0xf bound_ctrl:1
	v_add_f32_dpp v107, v107, v107 row_half_mirror row_mask:0xf bank_mask:0xf bound_ctrl:1
	s_nop 0
	v_add_f32_dpp v111, v111, v111 row_mirror row_mask:0xf bank_mask:0xf bound_ctrl:1
	v_add_f32_dpp v107, v107, v107 row_mirror row_mask:0xf bank_mask:0xf bound_ctrl:1
	s_nop 0
	v_readlane_b32 s37, v111, 16
	v_readlane_b32 s38, v111, 48
	v_readlane_b32 s16, v111, 0
	v_readlane_b32 s17, v111, 32
	v_mov_b32_e32 v112, s37
	v_mov_b32_e32 v113, s38
	v_pk_add_f32 v[112:113], s[16:17], v[112:113]
	v_add_f32_e32 v111, v112, v113
	s_waitcnt vmcnt(0)
	v_add_f32_e32 v102, v102, v111
	v_cmp_gt_f32_e32 vcc, v102, v106
	v_readlane_b32 s16, v107, 0
	v_readlane_b32 s37, v107, 16
	v_readlane_b32 s17, v107, 32
	v_readlane_b32 s38, v107, 48
	s_cbranch_vccnz .LBB0_801
	v_cmp_ngt_f32_e32 vcc, v102, v105
	s_cbranch_vccnz .LBB0_800
	s_mov_b32 s34, s36
	v_mov_b32_e32 v105, v102
